# baseline (speedup 1.0000x reference)
.LBB1_8:
	s_or_b64 exec, exec, s[4:5]
	s_waitcnt vmcnt(1)
	v_mov_b32_e32 v184, 1
	v_lshl_add_u32 v180, v176, 2, v172
	v_lshl_add_u32 v181, v177, 2, v172
	v_lshl_add_u32 v182, v178, 2, v172
	v_lshl_add_u32 v183, v179, 2, v172
	s_waitcnt lgkmcnt(0)
	ds_add_u32 v180, v184
	ds_add_u32 v181, v184
	ds_add_u32 v182, v184
	ds_add_u32 v183, v184
	s_waitcnt lgkmcnt(0)
	ds_read_b32 v151, v173
	s_waitcnt lgkmcnt(0)
	v_cvt_f32_i32_e32 v185, v151
	ds_write_b32 v173, v185 offset:256
	v_add_u32_e32 v10, v172, v2
	s_waitcnt vmcnt(1) lgkmcnt(0)
	s_barrier
	s_nop 0
	ds_read_b128 v[18:21], v10 offset:256
	ds_read_b128 v[22:25], v10 offset:288
	ds_read_b128 v[82:85], v10 offset:320
	ds_read_b128 v[86:89], v10 offset:352
	ds_read_b128 v[74:77], v10 offset:384
	ds_read_b128 v[78:81], v10 offset:416
	ds_read_b128 v[2:5], v213 offset:32768
	ds_read_b128 v[6:9], v213 offset:0
	ds_read_b128 v[66:69], v10 offset:448
	ds_read_b128 v[70:73], v10 offset:480
	ds_read_b128 v[10:13], v213 offset:1024
	s_waitcnt lgkmcnt(3)
	v_pk_mul_f32 v[26:27], v[8:9], v[20:21]
	v_pk_mul_f32 v[28:29], v[6:7], v[18:19]
	ds_read_b128 v[14:17], v213 offset:8192
	s_waitcnt lgkmcnt(1)
	v_pk_mul_f32 v[12:13], v[12:13], v[24:25]
	v_pk_mul_f32 v[10:11], v[10:11], v[22:23]
	v_pk_fma_f32 v[30:31], v[8:9], v[20:21], v[12:13]
	v_pk_fma_f32 v[32:33], v[6:7], v[18:19], v[10:11]
	v_cvt_pk_bf16_f32 v9, v12, v13
	v_cvt_pk_bf16_f32 v7, v26, v27
	v_cvt_pk_bf16_f32 v8, v10, v11
	v_cvt_pk_bf16_f32 v6, v28, v29
	ds_read_b128 v[10:13], v213 offset:33792
	s_nop 0
	v_mfma_f32_32x32x16_bf16 v[34:49], v[2:5], v[6:9], 0
	ds_read_b128 v[6:9], v213 offset:9216
	s_waitcnt lgkmcnt(2)
	v_mul_f32_e32 v26, v16, v20
	v_mul_f32_e32 v27, v17, v21
	v_pk_mul_f32 v[50:51], v[14:15], v[18:19]
	s_mov_b32 s4, 0x3727c5ac
	s_waitcnt lgkmcnt(0)
	v_pk_mul_f32 v[8:9], v[8:9], v[24:25]
	v_pk_mul_f32 v[28:29], v[6:7], v[22:23]
	v_pk_fma_f32 v[90:91], v[16:17], v[20:21], v[8:9]
	v_pk_fma_f32 v[92:93], v[14:15], v[18:19], v[28:29]
	ds_read_b128 v[14:17], v213 offset:2048
	v_cvt_pk_bf16_f32 v9, v8, v9
	v_cvt_pk_bf16_f32 v7, v26, v27
	v_cvt_pk_bf16_f32 v8, v28, v29
	ds_read_b128 v[26:29], v213 offset:3072
	v_cvt_pk_bf16_f32 v6, v50, v51
	s_waitcnt lgkmcnt(1)
	v_pk_mul_f32 v[94:95], v[14:15], v[82:83]
	s_mov_b32 s0, 0x3c800000
	v_mfma_f32_32x32x16_bf16 v[50:65], v[2:5], v[6:9], 0
	v_mul_f32_e32 v2, v16, v84
	v_mul_f32_e32 v3, v17, v85
	s_waitcnt lgkmcnt(0)
	v_mul_f32_e32 v4, v28, v88
	v_mul_f32_e32 v5, v29, v89
	v_pk_mul_f32 v[6:7], v[26:27], v[86:87]
	v_pk_fma_f32 v[8:9], v[16:17], v[84:85], v[4:5]
	v_cvt_pk_bf16_f32 v3, v2, v3
	v_pk_fma_f32 v[14:15], v[14:15], v[82:83], v[6:7]
	v_pk_add_f32 v[26:27], v[8:9], v[30:31]
	v_cvt_pk_bf16_f32 v5, v4, v5
	v_cvt_pk_bf16_f32 v4, v6, v7
	ds_read_b128 v[6:9], v213 offset:10240
	v_pk_add_f32 v[28:29], v[14:15], v[32:33]
	ds_read_b128 v[14:17], v213 offset:11264
	v_cvt_pk_bf16_f32 v2, v94, v95
	s_waitcnt lgkmcnt(1)
	v_pk_mul_f32 v[30:31], v[6:7], v[82:83]
	v_mov_b64_e32 v[152:153], s[4:5]
	v_mfma_f32_32x32x16_bf16 v[34:49], v[10:13], v[2:5], v[34:49]
	v_mul_f32_e32 v2, v8, v84
	v_mul_f32_e32 v3, v9, v85
	s_waitcnt lgkmcnt(0)
	v_mul_f32_e32 v4, v16, v88
	v_mul_f32_e32 v5, v17, v89
	v_pk_mul_f32 v[14:15], v[14:15], v[86:87]
	v_pk_fma_f32 v[8:9], v[8:9], v[84:85], v[4:5]
	v_pk_fma_f32 v[6:7], v[6:7], v[82:83], v[14:15]
	v_cvt_pk_bf16_f32 v5, v4, v5
	v_cvt_pk_bf16_f32 v3, v2, v3
	v_cvt_pk_bf16_f32 v4, v14, v15
	v_pk_add_f32 v[32:33], v[8:9], v[90:91]
	v_pk_add_f32 v[90:91], v[6:7], v[92:93]
	ds_read_b128 v[6:9], v213 offset:34816
	ds_read_b128 v[14:17], v213 offset:4096
	v_cvt_pk_bf16_f32 v2, v30, v31
	s_mov_b32 s13, 0
	s_mov_b64 s[6:7], 0
	v_mfma_f32_32x32x16_bf16 v[50:65], v[10:13], v[2:5], v[50:65]
	ds_read_b128 v[2:5], v213 offset:5120
	ds_read_b128 v[10:13], v213 offset:12288
	s_waitcnt lgkmcnt(2)
	v_pk_mul_f32 v[30:31], v[16:17], v[76:77]
	v_pk_mul_f32 v[92:93], v[14:15], v[74:75]
	s_waitcnt lgkmcnt(1)
	v_pk_mul_f32 v[4:5], v[4:5], v[80:81]
	v_pk_mul_f32 v[94:95], v[2:3], v[78:79]
	v_pk_fma_f32 v[2:3], v[16:17], v[76:77], v[4:5]
	v_cvt_pk_bf16_f32 v5, v4, v5
	v_pk_add_f32 v[96:97], v[2:3], v[26:27]
	v_cvt_pk_bf16_f32 v3, v30, v31
	v_cvt_pk_bf16_f32 v4, v94, v95
	v_cvt_pk_bf16_f32 v2, v92, v93
	v_pk_fma_f32 v[14:15], v[14:15], v[74:75], v[94:95]
	s_waitcnt lgkmcnt(0)
	v_pk_mul_f32 v[30:31], v[10:11], v[74:75]
	v_mfma_f32_32x32x16_bf16 v[34:49], v[6:9], v[2:5], v[34:49]
	ds_read_b128 v[2:5], v213 offset:13312
	v_add_f32_e32 v98, v14, v28
	v_add_f32_e32 v99, v15, v29
	ds_read_b128 v[14:17], v213 offset:35840
	v_pk_mul_f32 v[26:27], v[12:13], v[76:77]
	s_waitcnt lgkmcnt(1)
	v_pk_mul_f32 v[4:5], v[4:5], v[80:81]
	v_pk_mul_f32 v[28:29], v[2:3], v[78:79]
	v_pk_fma_f32 v[2:3], v[12:13], v[76:77], v[4:5]
	v_pk_fma_f32 v[10:11], v[10:11], v[74:75], v[28:29]
	v_pk_add_f32 v[32:33], v[2:3], v[32:33]
	v_pk_add_f32 v[92:93], v[10:11], v[90:91]
	ds_read_b128 v[10:13], v213 offset:6144
	v_cvt_pk_bf16_f32 v5, v4, v5
	v_cvt_pk_bf16_f32 v3, v26, v27
	v_cvt_pk_bf16_f32 v4, v28, v29
	ds_read_b128 v[26:29], v213 offset:7168
	v_cvt_pk_bf16_f32 v2, v30, v31
	s_waitcnt lgkmcnt(1)
	v_pk_mul_f32 v[30:31], v[10:11], v[66:67]
	v_mfma_f32_32x32x16_bf16 v[50:65], v[6:9], v[2:5], v[50:65]
	v_mul_f32_e32 v2, v12, v68
	v_mul_f32_e32 v3, v13, v69
	s_waitcnt lgkmcnt(0)
	v_mul_f32_e32 v4, v28, v72
	v_mul_f32_e32 v5, v29, v73
	v_pk_mul_f32 v[6:7], v[26:27], v[70:71]
	v_pk_fma_f32 v[8:9], v[12:13], v[68:69], v[4:5]
	v_cvt_pk_bf16_f32 v3, v2, v3
	v_pk_fma_f32 v[10:11], v[10:11], v[66:67], v[6:7]
	v_pk_add_f32 v[94:95], v[8:9], v[96:97]
	v_cvt_pk_bf16_f32 v5, v4, v5
	v_cvt_pk_bf16_f32 v4, v6, v7
	ds_read_b128 v[6:9], v213 offset:14336
	v_pk_add_f32 v[96:97], v[10:11], v[98:99]
	ds_read_b128 v[10:13], v213 offset:15360
	v_cvt_pk_bf16_f32 v2, v30, v31
	s_waitcnt lgkmcnt(1)
	v_pk_mul_f32 v[30:31], v[6:7], v[66:67]
	v_mfma_f32_32x32x16_bf16 v[34:49], v[14:17], v[2:5], v[34:49]
	s_waitcnt lgkmcnt(0)
	v_mul_f32_e32 v10, v10, v70
	v_mul_f32_e32 v11, v11, v71
	v_mul_f32_e32 v2, v8, v68
	v_mul_f32_e32 v3, v9, v69
	v_pk_mul_f32 v[4:5], v[12:13], v[72:73]
	v_pk_fma_f32 v[6:7], v[6:7], v[66:67], v[10:11]
	v_pk_fma_f32 v[8:9], v[8:9], v[68:69], v[4:5]
	v_pk_add_f32 v[92:93], v[6:7], v[92:93]
	v_cvt_pk_bf16_f32 v3, v2, v3
	v_pk_add_f32 v[90:91], v[8:9], v[32:33]
	v_cvt_pk_bf16_f32 v5, v4, v5
	v_cvt_pk_bf16_f32 v4, v10, v11
	ds_read_b128 v[26:29], v213 offset:36864
	ds_read_b128 v[6:9], v213 offset:16384
	v_cvt_pk_bf16_f32 v2, v30, v31
	ds_read_b128 v[98:101], v213 offset:25600
	ds_read_b128 v[102:105], v213 offset:37888
	v_mfma_f32_32x32x16_bf16 v[50:65], v[14:17], v[2:5], v[50:65]
	ds_read_b128 v[2:5], v213 offset:17408
	ds_read_b128 v[30:33], v213 offset:24576
	s_waitcnt lgkmcnt(4)
	v_pk_mul_f32 v[12:13], v[6:7], v[18:19]
	v_pk_mul_f32 v[10:11], v[8:9], v[20:21]
	s_waitcnt lgkmcnt(1)
	v_pk_mul_f32 v[14:15], v[2:3], v[22:23]
	v_pk_mul_f32 v[22:23], v[98:99], v[22:23]
	v_pk_fma_f32 v[112:113], v[6:7], v[18:19], v[14:15]
	s_waitcnt lgkmcnt(0)
	v_pk_mul_f32 v[114:115], v[30:31], v[18:19]
	v_pk_fma_f32 v[118:119], v[30:31], v[18:19], v[22:23]
	v_pk_mul_f32 v[4:5], v[4:5], v[24:25]
	v_pk_mul_f32 v[106:107], v[32:33], v[20:21]
	v_pk_mul_f32 v[24:25], v[100:101], v[24:25]
	ds_read_b128 v[98:101], v213 offset:18432
	v_cvt_pk_bf16_f32 v19, v106, v107
	ds_read_b128 v[106:109], v213 offset:19456
	v_pk_fma_f32 v[110:111], v[8:9], v[20:21], v[4:5]
	v_cvt_pk_bf16_f32 v5, v4, v5
	v_cvt_pk_bf16_f32 v3, v10, v11
	v_cvt_pk_bf16_f32 v4, v14, v15
	s_waitcnt lgkmcnt(0)
	v_pk_mul_f32 v[106:107], v[106:107], v[86:87]
	v_cvt_pk_bf16_f32 v2, v12, v13
	v_pk_mul_f32 v[120:121], v[98:99], v[82:83]
	v_pk_mul_f32 v[108:109], v[108:109], v[88:89]
	v_pk_fma_f32 v[98:99], v[98:99], v[82:83], v[106:107]
	v_mfma_f32_32x32x16_bf16 v[2:17], v[26:29], v[2:5], 0
	v_cvt_pk_bf16_f32 v18, v114, v115
	v_mul_f32_e32 v114, v100, v84
	v_mul_f32_e32 v115, v101, v85
	v_fma_f32 v100, v100, v84, v108
	v_fma_f32 v101, v101, v85, v109
	v_pk_add_f32 v[124:125], v[98:99], v[112:113]
	v_pk_add_f32 v[122:123], v[100:101], v[110:111]
	v_cvt_pk_bf16_f32 v101, v108, v109
	v_cvt_pk_bf16_f32 v100, v106, v107
	ds_read_b128 v[106:109], v213 offset:26624
	v_pk_fma_f32 v[116:117], v[32:33], v[20:21], v[24:25]
	v_cvt_pk_bf16_f32 v21, v24, v25
	v_cvt_pk_bf16_f32 v20, v22, v23
	ds_read_b128 v[110:113], v213 offset:27648
	v_cvt_pk_bf16_f32 v99, v114, v115
	v_mfma_f32_32x32x16_bf16 v[18:33], v[26:29], v[18:21], 0
	v_cvt_pk_bf16_f32 v98, v120, v121
	s_waitcnt lgkmcnt(1)
	v_mul_f32_e32 v114, v106, v82
	v_mul_f32_e32 v115, v107, v83
	s_waitcnt lgkmcnt(0)
	v_pk_mul_f32 v[86:87], v[110:111], v[86:87]
	v_pk_mul_f32 v[88:89], v[112:113], v[88:89]
	v_pk_fma_f32 v[82:83], v[106:107], v[82:83], v[86:87]
	v_mfma_f32_32x32x16_bf16 v[2:17], v[102:105], v[98:101], v[2:17]
	v_mul_f32_e32 v98, v108, v84
	v_mul_f32_e32 v99, v109, v85
	v_fma_f32 v84, v108, v84, v88
	v_fma_f32 v85, v109, v85, v89
	v_add_f32_e32 v108, v82, v118
	v_add_f32_e32 v109, v83, v119
	v_cvt_pk_bf16_f32 v83, v98, v99
	v_pk_add_f32 v[106:107], v[84:85], v[116:117]
	v_cvt_pk_bf16_f32 v85, v88, v89
	v_cvt_pk_bf16_f32 v84, v86, v87
	ds_read_b128 v[86:89], v213 offset:38912
	ds_read_b128 v[98:101], v213 offset:20480
	v_cvt_pk_bf16_f32 v82, v114, v115
	s_waitcnt lgkmcnt(0)
	v_pk_mul_f32 v[110:111], v[100:101], v[76:77]
	v_mfma_f32_32x32x16_bf16 v[18:33], v[102:105], v[82:85], v[18:33]
	ds_read_b128 v[82:85], v213 offset:21504
	ds_read_b128 v[102:105], v213 offset:28672
	v_mul_f32_e32 v112, v98, v74
	v_mul_f32_e32 v113, v99, v75
	s_waitcnt lgkmcnt(1)
	v_pk_mul_f32 v[84:85], v[84:85], v[80:81]
	v_pk_mul_f32 v[114:115], v[82:83], v[78:79]
	v_pk_fma_f32 v[82:83], v[100:101], v[76:77], v[84:85]
	v_cvt_pk_bf16_f32 v85, v84, v85
	v_pk_add_f32 v[116:117], v[82:83], v[122:123]
	v_cvt_pk_bf16_f32 v83, v110, v111
	v_cvt_pk_bf16_f32 v84, v114, v115
	v_cvt_pk_bf16_f32 v82, v112, v113
	v_pk_fma_f32 v[98:99], v[98:99], v[74:75], v[114:115]
	s_waitcnt lgkmcnt(0)
	v_pk_mul_f32 v[112:113], v[102:103], v[74:75]
	v_mfma_f32_32x32x16_bf16 v[2:17], v[86:89], v[82:85], v[2:17]
	ds_read_b128 v[82:85], v213 offset:29696
	v_add_f32_e32 v118, v98, v124
	v_add_f32_e32 v119, v99, v125
	v_mul_f32_e32 v110, v104, v76
	v_mul_f32_e32 v111, v105, v77
	ds_read_b128 v[98:101], v213 offset:39936
	s_waitcnt lgkmcnt(1)
	v_pk_mul_f32 v[78:79], v[82:83], v[78:79]
	v_pk_mul_f32 v[80:81], v[84:85], v[80:81]
	v_pk_fma_f32 v[74:75], v[102:103], v[74:75], v[78:79]
	v_pk_fma_f32 v[76:77], v[104:105], v[76:77], v[80:81]
	v_pk_add_f32 v[104:105], v[74:75], v[108:109]
	v_pk_add_f32 v[102:103], v[76:77], v[106:107]
	v_cvt_pk_bf16_f32 v77, v80, v81
	v_cvt_pk_bf16_f32 v76, v78, v79
	ds_read_b128 v[78:81], v213 offset:22528
	ds_read_b128 v[82:85], v213 offset:23552
	v_cvt_pk_bf16_f32 v75, v110, v111
	v_cvt_pk_bf16_f32 v74, v112, v113
	s_waitcnt lgkmcnt(0)
	v_pk_mul_f32 v[82:83], v[82:83], v[70:71]
	v_mfma_f32_32x32x16_bf16 v[18:33], v[86:89], v[74:77], v[18:33]
	v_mul_f32_e32 v74, v80, v68
	v_mul_f32_e32 v75, v81, v69
	v_mul_f32_e32 v76, v84, v72
	v_mul_f32_e32 v77, v85, v73
	v_mul_f32_e32 v86, v78, v66
	v_mul_f32_e32 v87, v79, v67
	v_pk_fma_f32 v[80:81], v[80:81], v[68:69], v[76:77]
	v_pk_fma_f32 v[78:79], v[78:79], v[66:67], v[82:83]
	v_cvt_pk_bf16_f32 v75, v74, v75
	v_pk_add_f32 v[88:89], v[80:81], v[116:117]
	v_pk_add_f32 v[106:107], v[78:79], v[118:119]
	ds_read_b128 v[78:81], v213 offset:30720
	v_cvt_pk_bf16_f32 v77, v76, v77
	v_cvt_pk_bf16_f32 v76, v82, v83
	ds_read_b128 v[82:85], v213 offset:31744
	v_cvt_pk_bf16_f32 v74, v86, v87
	s_waitcnt lgkmcnt(0)
	v_pk_mul_f32 v[72:73], v[84:85], v[72:73]
	v_mfma_f32_32x32x16_bf16 v[2:17], v[98:101], v[74:77], v[2:17]
	v_mul_f32_e32 v74, v80, v68
	v_mul_f32_e32 v75, v81, v69
	v_fma_f32 v68, v80, v68, v72
	v_fma_f32 v69, v81, v69, v73
	v_mul_f32_e32 v70, v82, v70
	v_mul_f32_e32 v71, v83, v71
	v_pk_add_f32 v[84:85], v[68:69], v[102:103]
	v_cvt_pk_bf16_f32 v69, v72, v73
	v_add_f32_e32 v72, v97, v96
	v_add_f32_e32 v73, v94, v95
	v_pk_mul_f32 v[76:77], v[78:79], v[66:67]
	v_pk_fma_f32 v[66:67], v[78:79], v[66:67], v[70:71]
	v_add_f32_e32 v72, v72, v73
	v_pk_add_f32 v[86:87], v[66:67], v[104:105]
	v_mov_b32_e32 v66, v72
	s_nop 1
	v_permlane32_swap_b32_e32 v72, v66
	v_add_f32_e32 v66, v72, v66
	v_cvt_pk_bf16_f32 v67, v74, v75
	v_rcp_f32_e32 v74, v66
	v_cvt_pk_bf16_f32 v68, v70, v71
	v_cvt_pk_bf16_f32 v66, v76, v77
	v_pk_mul_f32 v[70:71], v[46:47], v[74:75] op_sel_hi:[1,0]
	s_nop 0
	v_mfma_f32_32x32x16_bf16 v[18:33], v[98:101], v[66:69], v[18:33]
	v_mul_f32_e32 v66, v42, v74
	v_mul_f32_e32 v67, v43, v74
	v_add_f32_e32 v42, v93, v92
	v_add_f32_e32 v43, v90, v91
	v_pk_mul_f32 v[68:69], v[44:45], v[74:75] op_sel_hi:[1,0]
	v_add_f32_e32 v42, v42, v43
	v_mov_b32_e32 v43, v42
	s_nop 1
	v_permlane32_swap_b32_e32 v42, v43
	v_add_f32_e32 v42, v42, v43
	v_rcp_f32_e32 v42, v42
	v_add_f32_e32 v44, v107, v106
	v_add_f32_e32 v45, v88, v89
	v_pk_mul_f32 v[72:73], v[48:49], v[74:75] op_sel_hi:[1,0]
	v_add_f32_e32 v44, v44, v45
	v_pk_mul_f32 v[36:37], v[36:37], v[74:75] op_sel_hi:[1,0]
	v_pk_mul_f32 v[38:39], v[38:39], v[74:75] op_sel_hi:[1,0]
	v_pk_mul_f32 v[40:41], v[40:41], v[74:75] op_sel_hi:[1,0]
	v_pk_mul_f32 v[34:35], v[34:35], v[74:75] op_sel_hi:[1,0]
	v_pk_mul_f32 v[74:75], v[58:59], v[42:43] op_sel_hi:[1,0]
	v_pk_mul_f32 v[78:79], v[60:61], v[42:43] op_sel_hi:[1,0]
	v_pk_mul_f32 v[80:81], v[62:63], v[42:43] op_sel_hi:[1,0]
	v_pk_mul_f32 v[82:83], v[64:65], v[42:43] op_sel_hi:[1,0]
	v_pk_mul_f32 v[92:93], v[52:53], v[42:43] op_sel_hi:[1,0]
	v_mov_b32_e32 v43, v44
	s_nop 1
	v_permlane32_swap_b32_e32 v44, v43
	v_add_f32_e32 v43, v44, v43
	v_rcp_f32_e32 v76, v43
	v_pk_mul_f32 v[96:97], v[54:55], v[42:43] op_sel_hi:[1,0]
	v_pk_mul_f32 v[94:95], v[56:57], v[42:43] op_sel_hi:[1,0]
	v_pk_mul_f32 v[98:99], v[50:51], v[42:43] op_sel_hi:[1,0]
	v_pk_mul_f32 v[100:101], v[4:5], v[76:77] op_sel_hi:[1,0]
	v_pk_mov_b32 v[4:5], v[86:87], v[84:85] op_sel:[1,0]
	v_mov_b32_e32 v87, v85
	v_pk_add_f32 v[4:5], v[4:5], v[86:87]
	v_pk_mul_f32 v[102:103], v[6:7], v[76:77] op_sel_hi:[1,0]
	v_pk_add_f32 v[104:105], v[4:5], v[4:5] op_sel:[0,1] op_sel_hi:[1,0]
	v_cvt_pk_bf16_f32 v7, v40, v41
	ds_read_b128 v[84:87], v150 offset:52224
	ds_read_b128 v[50:53], v150 offset:35840
	ds_read_b128 v[54:57], v150 offset:36864
	ds_read_b128 v[58:61], v150 offset:37888
	ds_read_b128 v[62:65], v150 offset:38912
	v_cvt_pk_bf16_f32 v6, v38, v39
	v_cvt_pk_bf16_f32 v5, v36, v37
	v_cvt_pk_bf16_f32 v4, v34, v35
	ds_read_b128 v[88:91], v150 offset:53248
	ds_read_b128 v[34:37], v150 offset:39936
	ds_read_b128 v[38:41], v150 offset:40960
	ds_read_b128 v[42:45], v150 offset:41984
	ds_read_b128 v[46:49], v150 offset:43008
	v_cvt_pk_bf16_f32 v95, v94, v95
	v_cvt_pk_bf16_f32 v94, v96, v97
	v_cvt_pk_bf16_f32 v93, v92, v93
	v_cvt_pk_bf16_f32 v92, v98, v99
	s_waitcnt lgkmcnt(5)
	v_mfma_f32_32x32x16_bf16 v[50:65], v[84:87], v[4:7], v[50:65]
	v_mul_f32_e32 v10, v10, v76
	v_mul_f32_e32 v11, v11, v76
	v_mul_f32_e32 v12, v12, v76
	v_mul_f32_e32 v13, v13, v76
	v_mul_f32_e32 v8, v8, v76
	v_mul_f32_e32 v9, v9, v76
	v_mov_b32_e32 v77, v104
	s_nop 1
	v_permlane32_swap_b32_e32 v104, v77
	v_cvt_pk_bf16_f32 v73, v72, v73
	s_waitcnt lgkmcnt(0)
	v_mfma_f32_32x32x16_bf16 v[34:49], v[84:87], v[92:95], v[34:49]
	v_cvt_pk_bf16_f32 v72, v70, v71
	v_cvt_pk_bf16_f32 v70, v66, v67
	v_add_f32_e32 v66, v104, v77
	v_cvt_pk_bf16_f32 v71, v68, v69
	v_rcp_f32_e32 v104, v66
	v_cvt_pk_bf16_f32 v69, v82, v83
	v_cvt_pk_bf16_f32 v68, v80, v81
	v_cvt_pk_bf16_f32 v67, v78, v79
	v_cvt_pk_bf16_f32 v66, v74, v75
	ds_read_b128 v[78:81], v150 offset:54272
	v_mfma_f32_32x32x16_bf16 v[50:65], v[88:91], v[70:73], v[50:65]
	v_mul_f32_e32 v2, v2, v76
	v_mul_f32_e32 v3, v3, v76
	v_mul_f32_e32 v20, v20, v104
	v_mul_f32_e32 v21, v21, v104
	v_cvt_pk_bf16_f32 v85, v8, v9
	v_cvt_pk_bf16_f32 v82, v2, v3
	v_pk_mul_f32 v[2:3], v[22:23], v[104:105] op_sel_hi:[1,0]
	v_pk_mul_f32 v[8:9], v[24:25], v[104:105] op_sel_hi:[1,0]
	v_pk_mul_f32 v[18:19], v[18:19], v[104:105] op_sel_hi:[1,0]
	v_mfma_f32_32x32x16_bf16 v[34:49], v[88:91], v[66:69], v[34:49]
	v_cvt_pk_bf16_f32 v84, v102, v103
	v_cvt_pk_bf16_f32 v83, v100, v101
	ds_read_b128 v[86:89], v150 offset:55296
	v_cvt_pk_bf16_f32 v99, v8, v9
	v_cvt_pk_bf16_f32 v98, v2, v3
	v_cvt_pk_bf16_f32 v97, v20, v21
	v_cvt_pk_bf16_f32 v96, v18, v19
	s_waitcnt lgkmcnt(1)
	v_mfma_f32_32x32x16_bf16 v[50:65], v[78:81], v[82:85], v[50:65]
	v_mul_f32_e32 v2, v14, v76
	v_mul_f32_e32 v3, v15, v76
	v_mul_f32_e32 v8, v16, v76
	v_mul_f32_e32 v9, v17, v76
	v_mul_f32_e32 v14, v26, v104
	v_mul_f32_e32 v15, v27, v104
	v_cvt_pk_bf16_f32 v77, v8, v9
	v_cvt_pk_bf16_f32 v76, v2, v3
	v_cvt_pk_bf16_f32 v74, v10, v11
	v_pk_mul_f32 v[2:3], v[28:29], v[104:105] op_sel_hi:[1,0]
	v_mfma_f32_32x32x16_bf16 v[34:49], v[78:81], v[96:99], v[34:49]
	v_mul_f32_e32 v8, v30, v104
	v_mul_f32_e32 v9, v31, v104
	v_mul_f32_e32 v10, v32, v104
	v_mul_f32_e32 v11, v33, v104
	v_cvt_pk_bf16_f32 v75, v12, v13
	v_cvt_pk_bf16_f32 v81, v10, v11
	v_cvt_pk_bf16_f32 v80, v8, v9
	v_cvt_pk_bf16_f32 v79, v2, v3
	v_cvt_pk_bf16_f32 v78, v14, v15
	s_waitcnt lgkmcnt(0)
	v_mfma_f32_32x32x16_bf16 v[50:65], v[86:89], v[74:77], v[50:65]
	v_mfma_f32_32x32x16_bf16 v[34:49], v[86:89], v[78:81], v[34:49]
	ds_read_b128 v[86:89], v150 offset:56320
	ds_read_b128 v[18:21], v150 offset:44032
	ds_read_b128 v[22:25], v150 offset:45056
	ds_read_b128 v[26:29], v150 offset:46080
	ds_read_b128 v[30:33], v150 offset:47104
	ds_read_b128 v[100:103], v150 offset:57344
	s_waitcnt lgkmcnt(1)
	v_mfma_f32_32x32x16_bf16 v[18:33], v[86:89], v[4:7], v[18:33]
	ds_read_b128 v[2:5], v150 offset:48128
	ds_read_b128 v[6:9], v150 offset:49152
	ds_read_b128 v[10:13], v150 offset:50176
	ds_read_b128 v[14:17], v150 offset:51200
	s_waitcnt lgkmcnt(0)
	v_mfma_f32_32x32x16_bf16 v[2:17], v[86:89], v[92:95], v[2:17]
	v_mfma_f32_32x32x16_bf16 v[18:33], v[100:103], v[70:73], v[18:33]
	v_mfma_f32_32x32x16_bf16 v[2:17], v[100:103], v[66:69], v[2:17]
	ds_read_b128 v[66:69], v150 offset:58368
	ds_read_b128 v[70:73], v150 offset:59392
	s_waitcnt lgkmcnt(1)
	v_mfma_f32_32x32x16_bf16 v[18:33], v[66:69], v[82:85], v[18:33]
	v_mfma_f32_32x32x16_bf16 v[2:17], v[66:69], v[96:99], v[2:17]
	s_waitcnt lgkmcnt(0)
	v_mfma_f32_32x32x16_bf16 v[18:33], v[70:73], v[74:77], v[18:33]
	v_mfma_f32_32x32x16_bf16 v[2:17], v[70:73], v[78:81], v[2:17]
	s_nop 10
	v_mul_f32_e32 v66, v22, v22
	v_mul_f32_e32 v67, v23, v23
	v_mul_f32_e32 v68, v30, v30
	v_mul_f32_e32 v69, v31, v31
	v_mul_f32_e32 v70, v24, v24
	v_mul_f32_e32 v71, v25, v25
	v_pk_mul_f32 v[72:73], v[32:33], v[32:33]
	v_pk_mul_f32 v[74:75], v[20:21], v[20:21]
	v_pk_mul_f32 v[76:77], v[28:29], v[28:29]
	v_pk_mul_f32 v[78:79], v[26:27], v[26:27]
	v_pk_mul_f32 v[80:81], v[18:19], v[18:19]
	v_pk_fma_f32 v[78:79], v[58:59], v[58:59], v[78:79]
	v_pk_fma_f32 v[76:77], v[60:61], v[60:61], v[76:77]
	v_pk_fma_f32 v[74:75], v[52:53], v[52:53], v[74:75]
	v_pk_fma_f32 v[72:73], v[64:65], v[64:65], v[72:73]
	v_pk_fma_f32 v[70:71], v[56:57], v[56:57], v[70:71]
	v_pk_fma_f32 v[68:69], v[62:63], v[62:63], v[68:69]
	v_pk_fma_f32 v[66:67], v[54:55], v[54:55], v[66:67]
	v_pk_fma_f32 v[80:81], v[50:51], v[50:51], v[80:81]
	v_pk_add_f32 v[66:67], v[66:67], v[68:69]
	v_pk_add_f32 v[68:69], v[70:71], v[72:73]
	v_pk_add_f32 v[70:71], v[74:75], v[76:77]
	v_pk_add_f32 v[72:73], v[80:81], v[78:79]
	v_pk_add_f32 v[68:69], v[70:71], v[68:69]
	v_pk_add_f32 v[66:67], v[72:73], v[66:67]
	v_pk_mul_f32 v[72:73], v[14:15], v[14:15]
	v_pk_mov_b32 v[70:71], v[66:67], v[68:69] op_sel:[1,0]
	v_mov_b32_e32 v67, v69
	v_pk_add_f32 v[66:67], v[70:71], v[66:67]
	v_pk_mul_f32 v[70:71], v[6:7], v[6:7]
	v_pk_mul_f32 v[74:75], v[8:9], v[8:9]
	v_pk_mul_f32 v[76:77], v[16:17], v[16:17]
	v_pk_mul_f32 v[78:79], v[4:5], v[4:5]
	v_pk_mul_f32 v[80:81], v[12:13], v[12:13]
	v_pk_mul_f32 v[82:83], v[10:11], v[10:11]
	v_pk_mul_f32 v[84:85], v[2:3], v[2:3]
	v_pk_fma_f32 v[82:83], v[42:43], v[42:43], v[82:83]
	v_pk_fma_f32 v[80:81], v[44:45], v[44:45], v[80:81]
	v_pk_fma_f32 v[78:79], v[36:37], v[36:37], v[78:79]
	v_pk_fma_f32 v[76:77], v[48:49], v[48:49], v[76:77]
	v_pk_fma_f32 v[74:75], v[40:41], v[40:41], v[74:75]
	v_pk_fma_f32 v[72:73], v[46:47], v[46:47], v[72:73]
	v_pk_fma_f32 v[70:71], v[38:39], v[38:39], v[70:71]
	v_pk_fma_f32 v[84:85], v[34:35], v[34:35], v[84:85]
	v_pk_add_f32 v[70:71], v[70:71], v[72:73]
	v_pk_add_f32 v[72:73], v[74:75], v[76:77]
	v_pk_add_f32 v[74:75], v[78:79], v[80:81]
	v_pk_add_f32 v[76:77], v[84:85], v[82:83]
	v_pk_add_f32 v[72:73], v[74:75], v[72:73]
	v_pk_add_f32 v[70:71], v[76:77], v[70:71]
	v_pk_add_f32 v[66:67], v[66:67], v[66:67] op_sel:[0,1] op_sel_hi:[1,0]
	v_add_f32_e32 v70, v71, v70
	v_add_f32_e32 v71, v72, v73
	v_mov_b32_e32 v69, v66
	v_add_f32_e32 v70, v70, v71
	s_nop 0
	v_permlane32_swap_b32_e32 v66, v69
	v_mov_b32_e32 v68, v70
	s_nop 1
	v_permlane32_swap_b32_e32 v70, v68
	v_mov_b32_e32 v71, v66
	v_pk_add_f32 v[66:67], v[70:71], v[68:69]
	v_pk_fma_f32 v[66:67], v[66:67], s[0:1], v[152:153] op_sel_hi:[1,0,0]
	s_mov_b32 s1, 0x800000
	v_rsq_f32_e32 v68, v67
	s_nop 0
	v_pk_mul_f32 v[158:159], v[50:51], v[68:69] op_sel_hi:[1,0]
	v_pk_mul_f32 v[50:51], v[18:19], v[68:69] op_sel_hi:[1,0]
	v_pk_mul_f32 v[80:81], v[60:61], v[68:69] op_sel_hi:[1,0]
	v_pk_mul_f32 v[60:61], v[28:29], v[68:69] op_sel_hi:[1,0]
	v_pk_mul_f32 v[78:79], v[58:59], v[68:69] op_sel_hi:[1,0]
	v_pk_mul_f32 v[160:161], v[52:53], v[68:69] op_sel_hi:[1,0]
	v_pk_mul_f32 v[82:83], v[54:55], v[68:69] op_sel_hi:[1,0]
	v_rsq_f32_e32 v28, v66
	v_pk_mul_f32 v[168:169], v[56:57], v[68:69] op_sel_hi:[1,0]
	v_pk_mul_f32 v[58:59], v[26:27], v[68:69] op_sel_hi:[1,0]
	v_pk_mul_f32 v[52:53], v[20:21], v[68:69] op_sel_hi:[1,0]
	v_pk_mul_f32 v[54:55], v[22:23], v[68:69] op_sel_hi:[1,0]
	v_pk_mul_f32 v[56:57], v[24:25], v[68:69] op_sel_hi:[1,0]
	v_pk_mul_f32 v[18:19], v[42:43], v[28:29] op_sel_hi:[1,0]
	v_pk_mul_f32 v[20:21], v[44:45], v[28:29] op_sel_hi:[1,0]
	v_pk_mul_f32 v[22:23], v[46:47], v[28:29] op_sel_hi:[1,0]
	v_pk_mul_f32 v[26:27], v[48:49], v[28:29] op_sel_hi:[1,0]
	v_pk_mul_f32 v[162:163], v[34:35], v[28:29] op_sel_hi:[1,0]
	v_pk_mul_f32 v[164:165], v[36:37], v[28:29] op_sel_hi:[1,0]
	v_pk_mul_f32 v[166:167], v[38:39], v[28:29] op_sel_hi:[1,0]
	v_pk_mul_f32 v[24:25], v[40:41], v[28:29] op_sel_hi:[1,0]
	v_pk_mul_f32 v[104:105], v[2:3], v[28:29] op_sel_hi:[1,0]
	v_pk_mul_f32 v[112:113], v[4:5], v[28:29] op_sel_hi:[1,0]
	ds_read_b128 v[2:5], v150 offset:60416
	ds_read_b128 v[34:37], v174 offset:32768
	ds_read_b128 v[38:41], v174 offset:32800
	ds_read_b128 v[42:45], v174 offset:32832
	ds_read_b128 v[46:49], v174 offset:32864
	v_cvt_pk_bf16_f32 v129, v168, v169
	v_cvt_pk_bf16_f32 v128, v82, v83
	v_cvt_pk_bf16_f32 v127, v160, v161
	v_cvt_pk_bf16_f32 v126, v158, v159
	v_cvt_pk_bf16_f32 v137, v24, v25
	v_cvt_pk_bf16_f32 v136, v166, v167
	v_cvt_pk_bf16_f32 v135, v164, v165
	s_waitcnt lgkmcnt(0)
	v_mfma_f32_32x32x16_bf16 v[86:101], v[2:5], v[126:129], v[34:49]
	v_cvt_pk_bf16_f32 v134, v162, v163
	v_mul_f32_e32 v84, v62, v68
	v_mul_f32_e32 v85, v63, v68
	v_mul_f32_e32 v170, v64, v68
	v_mul_f32_e32 v171, v65, v68
	v_pk_mul_f32 v[62:63], v[30:31], v[68:69] op_sel_hi:[1,0]
	v_pk_mul_f32 v[64:65], v[32:33], v[68:69] op_sel_hi:[1,0]
	v_pk_mul_f32 v[116:117], v[6:7], v[28:29] op_sel_hi:[1,0]
	v_pk_mul_f32 v[154:155], v[8:9], v[28:29] op_sel_hi:[1,0]
	v_mfma_f32_32x32x16_bf16 v[34:49], v[2:5], v[134:137], v[34:49]
	ds_read_b128 v[6:9], v150 offset:61440
	ds_read_b128 v[66:69], v174 offset:32896
	ds_read_b128 v[106:109], v150 offset:64512
	v_cvt_pk_bf16_f32 v125, v170, v171
	v_cvt_pk_bf16_f32 v124, v84, v85
	v_cvt_pk_bf16_f32 v123, v80, v81
	v_cvt_pk_bf16_f32 v122, v78, v79
	v_cvt_pk_bf16_f32 v149, v26, v27
	v_cvt_pk_bf16_f32 v148, v22, v23
	v_cvt_pk_bf16_f32 v147, v20, v21
	v_cvt_pk_bf16_f32 v146, v18, v19
	s_waitcnt lgkmcnt(2)
	v_mfma_f32_32x32x16_bf16 v[86:101], v[6:9], v[122:125], v[86:101]
	v_mul_f32_e32 v102, v10, v28
	v_mul_f32_e32 v103, v11, v28
	v_mul_f32_e32 v110, v12, v28
	v_mul_f32_e32 v111, v13, v28
	v_mul_f32_e32 v114, v14, v28
	v_mul_f32_e32 v115, v15, v28
	v_pk_mul_f32 v[156:157], v[16:17], v[28:29] op_sel_hi:[1,0]
	ds_read_b128 v[176:179], v174 offset:33536
	ds_read_b128 v[180:183], v174 offset:33568
	ds_read_b128 v[184:187], v174 offset:33600
	ds_read_b128 v[28:31], v174 offset:33632
	ds_read_b128 v[188:191], v174 offset:33792
	ds_read_b128 v[192:195], v174 offset:33824
	ds_read_b128 v[196:199], v174 offset:33856
	ds_read_b128 v[200:203], v174 offset:33888
	ds_read_b128 v[204:207], v150 offset:62464
	v_cvt_pk_bf16_f32 v133, v56, v57
	v_mfma_f32_32x32x16_bf16 v[34:49], v[6:9], v[146:149], v[34:49]
	v_cvt_pk_bf16_f32 v132, v54, v55
	v_cvt_pk_bf16_f32 v131, v52, v53
	v_cvt_pk_bf16_f32 v130, v50, v51
	ds_read_b128 v[70:73], v174 offset:33664
	ds_read_b128 v[74:77], v174 offset:33920
	ds_read_b128 v[208:211], v150 offset:63488
	v_cvt_pk_bf16_f32 v145, v154, v155
	v_cvt_pk_bf16_f32 v144, v116, v117
	v_cvt_pk_bf16_f32 v143, v112, v113
	v_cvt_pk_bf16_f32 v142, v104, v105
	s_waitcnt lgkmcnt(3)
	v_mfma_f32_32x32x16_bf16 v[86:101], v[204:207], v[130:133], v[86:101]
	v_cvt_pk_bf16_f32 v121, v64, v65
	v_cvt_pk_bf16_f32 v120, v62, v63
	v_cvt_pk_bf16_f32 v119, v60, v61
	v_cvt_pk_bf16_f32 v118, v58, v59
	v_cvt_pk_bf16_f32 v141, v156, v157
	v_cvt_pk_bf16_f32 v140, v114, v115
	v_cvt_pk_bf16_f32 v139, v110, v111
	v_mfma_f32_32x32x16_bf16 v[34:49], v[204:207], v[142:145], v[34:49]
	v_cvt_pk_bf16_f32 v138, v102, v103
	v_fma_f32 v16, v30, v170, v202
	v_fma_f32 v17, v31, v171, v203
	v_fma_f32 v14, v28, v84, v200
	v_fma_f32 v15, v29, v85, v201
	v_pk_fma_f32 v[12:13], v[186:187], v[80:81], v[198:199]
	v_pk_fma_f32 v[10:11], v[184:185], v[78:79], v[196:197]
	v_pk_fma_f32 v[8:9], v[182:183], v[168:169], v[194:195]
	s_waitcnt lgkmcnt(0)
	v_mfma_f32_32x32x16_bf16 v[86:101], v[208:211], v[118:121], v[86:101]
	v_fma_f32 v6, v180, v82, v192
	v_fma_f32 v7, v181, v83, v193
	ds_read_b128 v[78:81], v174 offset:33760
	ds_read_b128 v[82:85], v174 offset:33248
	v_fma_f32 v4, v178, v160, v190
	v_fma_f32 v5, v179, v161, v191
	v_pk_fma_f32 v[2:3], v[176:177], v[158:159], v[188:189]
	v_pk_fma_f32 v[32:33], v[30:31], v[26:27], v[202:203]
	v_pk_fma_f32 v[30:31], v[28:29], v[22:23], v[200:201]
	v_pk_fma_f32 v[28:29], v[186:187], v[20:21], v[198:199]
	v_pk_fma_f32 v[26:27], v[184:185], v[18:19], v[196:197]
	v_pk_fma_f32 v[24:25], v[182:183], v[24:25], v[194:195]
	v_pk_fma_f32 v[22:23], v[180:181], v[166:167], v[192:193]
	v_pk_fma_f32 v[20:21], v[178:179], v[164:165], v[190:191]
	v_pk_fma_f32 v[18:19], v[176:177], v[162:163], v[188:189]
	ds_read_b128 v[158:161], v174 offset:33696
	ds_read_b128 v[162:165], v174 offset:33728
	ds_read_b128 v[166:169], v174 offset:33952
	ds_read_b128 v[176:179], v174 offset:33984
	ds_read_b128 v[180:183], v174 offset:34016
	ds_read_b128 v[184:187], v212 offset:11264
	v_mfma_f32_32x32x16_bf16 v[34:49], v[208:211], v[138:141], v[34:49]
	v_cvt_pk_bf16_f32 v86, v86, v87
	v_cvt_pk_bf16_f32 v87, v88, v89
	v_cvt_pk_bf16_f32 v88, v90, v91
	v_cvt_pk_bf16_f32 v89, v92, v93
	ds_read_b128 v[90:93], v212 offset:12288
	v_pk_max_i16 v86, v86, 0
	v_pk_max_i16 v87, v87, 0
	v_pk_max_i16 v88, v88, 0
	v_pk_max_i16 v89, v89, 0
	s_nop 1
	s_nop 0
	v_cvt_pk_bf16_f32 v188, v34, v35
	v_cvt_pk_bf16_f32 v189, v36, v37
	v_cvt_pk_bf16_f32 v190, v38, v39
	v_cvt_pk_bf16_f32 v191, v40, v41
	s_waitcnt lgkmcnt(1)
	v_mfma_f32_32x32x16_bf16 v[2:17], v[184:187], v[86:89], v[2:17]
	v_pk_max_i16 v188, v188, 0
	v_pk_max_i16 v189, v189, 0
	v_pk_max_i16 v190, v190, 0
	v_pk_max_i16 v191, v191, 0
	v_cvt_pk_bf16_f32 v94, v94, v95
	v_cvt_pk_bf16_f32 v95, v96, v97
	v_cvt_pk_bf16_f32 v96, v98, v99
	v_cvt_pk_bf16_f32 v97, v100, v101
	v_cvt_pk_bf16_f32 v98, v42, v43
	v_cvt_pk_bf16_f32 v99, v44, v45
	v_mfma_f32_32x32x16_bf16 v[18:33], v[184:187], v[188:191], v[18:33]
	ds_read_b128 v[184:187], v212 offset:19456
	v_cvt_pk_bf16_f32 v100, v46, v47
	v_cvt_pk_bf16_f32 v101, v48, v49
	v_fma_f32 v64, v80, v64, v182
	v_fma_f32 v65, v81, v65, v183
	v_pk_fma_f32 v[62:63], v[78:79], v[62:63], v[180:181]
	v_pk_fma_f32 v[60:61], v[164:165], v[60:61], v[178:179]
	v_pk_fma_f32 v[58:59], v[162:163], v[58:59], v[176:177]
	v_pk_max_i16 v94, v94, 0
	v_pk_max_i16 v95, v95, 0
	v_pk_max_i16 v96, v96, 0
	v_pk_max_i16 v97, v97, 0
	v_pk_max_i16 v98, v98, 0
	v_pk_max_i16 v99, v99, 0
	v_pk_max_i16 v100, v100, 0
	v_pk_max_i16 v101, v101, 0
	v_pk_fma_f32 v[56:57], v[160:161], v[56:57], v[168:169]
	s_waitcnt lgkmcnt(1)
	v_mfma_f32_32x32x16_bf16 v[2:17], v[90:93], v[94:97], v[2:17]
	v_fma_f32 v54, v158, v54, v166
	v_fma_f32 v55, v159, v55, v167
	v_fma_f32 v52, v72, v52, v76
	v_fma_f32 v53, v73, v53, v77
	v_fma_f32 v50, v70, v50, v74
	v_fma_f32 v51, v71, v51, v75
	v_pk_fma_f32 v[48:49], v[80:81], v[156:157], v[182:183]
	v_pk_fma_f32 v[46:47], v[78:79], v[114:115], v[180:181]
	v_pk_fma_f32 v[44:45], v[164:165], v[110:111], v[178:179]
	v_pk_fma_f32 v[42:43], v[162:163], v[102:103], v[176:177]
	v_mfma_f32_32x32x16_bf16 v[18:33], v[90:93], v[98:101], v[18:33]
	ds_read_b128 v[90:93], v212 offset:20480
	v_fma_f32 v40, v160, v154, v168
	v_fma_f32 v41, v161, v155, v169
	v_fma_f32 v38, v158, v116, v166
	v_fma_f32 v39, v159, v117, v167
	v_pk_fma_f32 v[36:37], v[72:73], v[112:113], v[76:77]
	v_pk_fma_f32 v[34:35], v[70:71], v[104:105], v[74:75]
	s_waitcnt lgkmcnt(1)
	v_mfma_f32_32x32x16_bf16 v[50:65], v[184:187], v[86:89], v[50:65]
	ds_read_b128 v[70:73], v174 offset:32928
	ds_read_b128 v[74:77], v174 offset:32960
	ds_read_b128 v[78:81], v174 offset:32992
	ds_read_b128 v[86:89], v174 offset:33024
	ds_read_b128 v[110:113], v212 offset:1024
	v_mfma_f32_32x32x16_bf16 v[34:49], v[184:187], v[188:191], v[34:49]
	s_waitcnt lgkmcnt(5)
	v_mfma_f32_32x32x16_bf16 v[50:65], v[90:93], v[94:97], v[50:65]
	v_mfma_f32_32x32x16_bf16 v[34:49], v[90:93], v[98:101], v[34:49]
	s_waitcnt lgkmcnt(2)
	v_mfma_f32_32x32x16_bf16 v[90:105], v[106:109], v[126:129], v[66:81]
	v_mfma_f32_32x32x16_bf16 v[66:81], v[106:109], v[134:137], v[66:81]
	ds_read_b128 v[106:109], v212 offset:0
	s_waitcnt lgkmcnt(0)
	v_mfma_f32_32x32x16_bf16 v[90:105], v[106:109], v[122:125], v[90:105]
	v_mfma_f32_32x32x16_bf16 v[66:81], v[106:109], v[146:149], v[66:81]
	ds_read_b128 v[106:109], v212 offset:2048
	v_mfma_f32_32x32x16_bf16 v[90:105], v[110:113], v[130:133], v[90:105]
	v_mfma_f32_32x32x16_bf16 v[66:81], v[110:113], v[142:145], v[66:81]
	ds_read_b128 v[110:113], v212 offset:13312
	s_waitcnt lgkmcnt(1)
	v_mfma_f32_32x32x16_bf16 v[90:105], v[106:109], v[118:121], v[90:105]
	v_mfma_f32_32x32x16_bf16 v[66:81], v[106:109], v[138:141], v[66:81]
	s_nop 10
	v_cvt_pk_bf16_f32 v90, v90, v91
	v_cvt_pk_bf16_f32 v91, v92, v93
	v_cvt_pk_bf16_f32 v92, v94, v95
	v_cvt_pk_bf16_f32 v94, v98, v99
	v_cvt_pk_bf16_f32 v95, v100, v101
	ds_read_b128 v[98:101], v212 offset:21504
	v_cvt_pk_bf16_f32 v66, v66, v67
	v_cvt_pk_bf16_f32 v67, v68, v69
	v_cvt_pk_bf16_f32 v68, v70, v71
	v_cvt_pk_bf16_f32 v93, v96, v97
	v_cvt_pk_bf16_f32 v69, v72, v73
	ds_read_b128 v[70:73], v212 offset:14336
	v_pk_max_i16 v90, v90, 0
	v_pk_max_i16 v91, v91, 0
	v_pk_max_i16 v92, v92, 0
	v_pk_max_i16 v93, v93, 0
	v_pk_max_i16 v66, v66, 0
	v_pk_max_i16 v67, v67, 0
	v_pk_max_i16 v68, v68, 0
	v_pk_max_i16 v69, v69, 0
	v_cvt_pk_bf16_f32 v96, v102, v103
	s_waitcnt lgkmcnt(2)
	v_mfma_f32_32x32x16_bf16 v[2:17], v[110:113], v[90:93], v[2:17]
	v_cvt_pk_bf16_f32 v97, v104, v105
	v_cvt_pk_bf16_f32 v74, v74, v75
	v_cvt_pk_bf16_f32 v75, v76, v77
	v_cvt_pk_bf16_f32 v76, v78, v79
	v_cvt_pk_bf16_f32 v77, v80, v81
	v_pk_max_i16 v94, v94, 0
	v_pk_max_i16 v95, v95, 0
	v_pk_max_i16 v96, v96, 0
	v_pk_max_i16 v97, v97, 0
	v_pk_max_i16 v74, v74, 0
	v_pk_max_i16 v75, v75, 0
	v_pk_max_i16 v76, v76, 0
	v_pk_max_i16 v77, v77, 0
	v_mfma_f32_32x32x16_bf16 v[18:33], v[110:113], v[66:69], v[18:33]
	s_waitcnt lgkmcnt(1)
	v_mfma_f32_32x32x16_bf16 v[34:49], v[98:101], v[66:69], v[34:49]
	ds_read_b128 v[66:69], v212 offset:22528
	v_mfma_f32_32x32x16_bf16 v[50:65], v[98:101], v[90:93], v[50:65]
	s_waitcnt lgkmcnt(1)
	v_mfma_f32_32x32x16_bf16 v[2:17], v[70:73], v[94:97], v[2:17]
	v_mfma_f32_32x32x16_bf16 v[18:33], v[70:73], v[74:77], v[18:33]
	ds_read_b128 v[78:81], v212 offset:3072
	s_waitcnt lgkmcnt(1)
	v_mfma_f32_32x32x16_bf16 v[50:65], v[66:69], v[94:97], v[50:65]
	ds_read_b128 v[90:93], v174 offset:33056
	ds_read_b128 v[94:97], v174 offset:33088
	ds_read_b128 v[98:101], v174 offset:33120
	ds_read_b128 v[70:73], v174 offset:33152
	v_mfma_f32_32x32x16_bf16 v[34:49], v[66:69], v[74:77], v[34:49]
	ds_read_b128 v[66:69], v212 offset:4096
	ds_read_b128 v[74:77], v212 offset:5120
	s_waitcnt lgkmcnt(3)
	v_mfma_f32_32x32x16_bf16 v[102:117], v[78:81], v[126:129], v[86:101]
	v_mfma_f32_32x32x16_bf16 v[86:101], v[78:81], v[134:137], v[86:101]
	s_waitcnt lgkmcnt(1)
	v_mfma_f32_32x32x16_bf16 v[86:101], v[66:69], v[146:149], v[86:101]
	v_mfma_f32_32x32x16_bf16 v[102:117], v[66:69], v[122:125], v[102:117]
	ds_read_b128 v[66:69], v212 offset:6144
	s_waitcnt lgkmcnt(1)
	v_mfma_f32_32x32x16_bf16 v[86:101], v[74:77], v[142:145], v[86:101]
	v_mfma_f32_32x32x16_bf16 v[102:117], v[74:77], v[130:133], v[102:117]
	ds_read_b128 v[74:77], v212 offset:15360
	s_waitcnt lgkmcnt(1)
	v_mfma_f32_32x32x16_bf16 v[86:101], v[66:69], v[138:141], v[86:101]
	v_mfma_f32_32x32x16_bf16 v[102:117], v[66:69], v[118:121], v[102:117]
	s_nop 10
	v_cvt_pk_bf16_f32 v78, v86, v87
	v_cvt_pk_bf16_f32 v80, v90, v91
	v_cvt_pk_bf16_f32 v79, v88, v89
	v_cvt_pk_bf16_f32 v81, v92, v93
	ds_read_b128 v[86:89], v212 offset:16384
	ds_read_b128 v[90:93], v212 offset:23552
	v_cvt_pk_bf16_f32 v66, v102, v103
	v_cvt_pk_bf16_f32 v67, v104, v105
	v_cvt_pk_bf16_f32 v68, v106, v107
	v_cvt_pk_bf16_f32 v69, v108, v109
	v_pk_max_i16 v66, v66, 0
	v_pk_max_i16 v67, v67, 0
	v_pk_max_i16 v68, v68, 0
	v_pk_max_i16 v69, v69, 0
	v_pk_max_i16 v78, v78, 0
	v_pk_max_i16 v79, v79, 0
	v_pk_max_i16 v80, v80, 0
	v_pk_max_i16 v81, v81, 0
	v_cvt_pk_bf16_f32 v94, v94, v95
	s_waitcnt lgkmcnt(2)
	v_mfma_f32_32x32x16_bf16 v[18:33], v[74:77], v[78:81], v[18:33]
	v_cvt_pk_bf16_f32 v95, v96, v97
	v_cvt_pk_bf16_f32 v96, v98, v99
	v_cvt_pk_bf16_f32 v97, v100, v101
	v_pk_max_i16 v94, v94, 0
	v_pk_max_i16 v95, v95, 0
	v_pk_max_i16 v96, v96, 0
	v_pk_max_i16 v97, v97, 0
	v_mfma_f32_32x32x16_bf16 v[2:17], v[74:77], v[66:69], v[2:17]
	v_cvt_pk_bf16_f32 v74, v110, v111
	v_cvt_pk_bf16_f32 v75, v112, v113
	v_cvt_pk_bf16_f32 v76, v114, v115
	v_cvt_pk_bf16_f32 v77, v116, v117
	v_pk_max_i16 v74, v74, 0
	v_pk_max_i16 v75, v75, 0
	v_pk_max_i16 v76, v76, 0
	v_pk_max_i16 v77, v77, 0
	s_waitcnt lgkmcnt(0)
	v_mfma_f32_32x32x16_bf16 v[50:65], v[90:93], v[66:69], v[50:65]
	ds_read_b128 v[66:69], v212 offset:24576
	v_mfma_f32_32x32x16_bf16 v[34:49], v[90:93], v[78:81], v[34:49]
	ds_read_b128 v[102:105], v212 offset:7168
	v_mfma_f32_32x32x16_bf16 v[2:17], v[86:89], v[74:77], v[2:17]
	s_waitcnt lgkmcnt(1)
	v_mfma_f32_32x32x16_bf16 v[50:65], v[66:69], v[74:77], v[50:65]
	ds_read_b128 v[74:77], v174 offset:33184
	ds_read_b128 v[78:81], v174 offset:33216
	v_mfma_f32_32x32x16_bf16 v[34:49], v[66:69], v[94:97], v[34:49]
	ds_read_b128 v[66:69], v212 offset:8192
	v_mfma_f32_32x32x16_bf16 v[18:33], v[86:89], v[94:97], v[18:33]
	s_waitcnt lgkmcnt(1)
	v_mfma_f32_32x32x16_bf16 v[86:101], v[102:105], v[126:129], v[70:85]
	v_mfma_f32_32x32x16_bf16 v[70:85], v[102:105], v[134:137], v[70:85]
	ds_read_b128 v[102:105], v212 offset:9216
	v_lshlrev_b32_e32 v135, 2, v1
	v_add_u32_e32 v134, v172, v174
	s_waitcnt lgkmcnt(1)
	v_mfma_f32_32x32x16_bf16 v[86:101], v[66:69], v[122:125], v[86:101]
	v_mfma_f32_32x32x16_bf16 v[70:85], v[66:69], v[146:149], v[70:85]
	ds_read_b128 v[66:69], v212 offset:10240
	s_waitcnt lgkmcnt(1)
	v_mfma_f32_32x32x16_bf16 v[86:101], v[102:105], v[130:133], v[86:101]
	v_mfma_f32_32x32x16_bf16 v[70:85], v[102:105], v[142:145], v[70:85]
	ds_read_b128 v[102:105], v212 offset:17408
	s_waitcnt lgkmcnt(1)
	v_mfma_f32_32x32x16_bf16 v[86:101], v[66:69], v[118:121], v[86:101]
	v_mfma_f32_32x32x16_bf16 v[70:85], v[66:69], v[138:141], v[70:85]
	s_nop 10
	v_cvt_pk_bf16_f32 v68, v90, v91
	v_cvt_pk_bf16_f32 v69, v92, v93
	ds_read_b128 v[90:93], v212 offset:25600
	v_cvt_pk_bf16_f32 v66, v86, v87
	v_cvt_pk_bf16_f32 v67, v88, v89
	v_pk_max_i16 v66, v66, 0
	v_pk_max_i16 v67, v67, 0
	v_pk_max_i16 v68, v68, 0
	v_pk_max_i16 v69, v69, 0
	v_cvt_pk_bf16_f32 v70, v70, v71
	v_cvt_pk_bf16_f32 v71, v72, v73
	s_waitcnt lgkmcnt(1)
	v_mfma_f32_32x32x16_bf16 v[2:17], v[102:105], v[66:69], v[2:17]
	v_cvt_pk_bf16_f32 v72, v74, v75
	v_cvt_pk_bf16_f32 v73, v76, v77
	ds_read_b128 v[74:77], v212 offset:18432
	v_cvt_pk_bf16_f32 v86, v94, v95
	v_cvt_pk_bf16_f32 v87, v96, v97
	v_cvt_pk_bf16_f32 v88, v98, v99
	s_waitcnt lgkmcnt(1)
	v_mfma_f32_32x32x16_bf16 v[50:65], v[90:93], v[66:69], v[50:65]
	ds_read_b128 v[66:69], v212 offset:26624
	v_cvt_pk_bf16_f32 v89, v100, v101
	v_pk_max_i16 v86, v86, 0
	v_pk_max_i16 v87, v87, 0
	v_pk_max_i16 v88, v88, 0
	v_pk_max_i16 v89, v89, 0
	v_pk_max_i16 v70, v70, 0
	v_pk_max_i16 v71, v71, 0
	v_pk_max_i16 v72, v72, 0
	v_pk_max_i16 v73, v73, 0
	v_cvt_pk_bf16_f32 v78, v78, v79
	v_cvt_pk_bf16_f32 v79, v80, v81
	s_waitcnt lgkmcnt(1)
	v_mfma_f32_32x32x16_bf16 v[2:17], v[74:77], v[86:89], v[2:17]
	v_cvt_pk_bf16_f32 v80, v82, v83
	v_cvt_pk_bf16_f32 v81, v84, v85
	v_pk_max_i16 v78, v78, 0
	v_pk_max_i16 v79, v79, 0
	v_pk_max_i16 v80, v80, 0
	v_pk_max_i16 v81, v81, 0
	s_waitcnt lgkmcnt(0)
	v_mfma_f32_32x32x16_bf16 v[50:65], v[66:69], v[86:89], v[50:65]
	v_mfma_f32_32x32x16_bf16 v[34:49], v[90:93], v[70:73], v[34:49]
	s_nop 10
	v_add_f32_e32 v130, v10, v58
	v_add_f32_e32 v131, v11, v59
	v_add_f32_e32 v132, v12, v60
	v_add_f32_e32 v133, v13, v61
	v_add_f32_e32 v138, v4, v52
	v_add_f32_e32 v139, v5, v53
	v_pk_add_f32 v[140:141], v[16:17], v[64:65]
	v_pk_add_f32 v[142:143], v[8:9], v[56:57]
	v_pk_add_f32 v[144:145], v[14:15], v[62:63]
	v_pk_add_f32 v[146:147], v[6:7], v[54:55]
	v_mfma_f32_32x32x16_bf16 v[18:33], v[102:105], v[70:73], v[18:33]
	ds_read2st64_b32 v[70:71], v135 offset0:133 offset1:134
	v_add_f32_e32 v148, v2, v50
	v_add_f32_e32 v149, v3, v51
	v_add_f32_e32 v144, v146, v144
	v_add_f32_e32 v145, v147, v145
	v_pk_add_f32 v[140:141], v[142:143], v[140:141]
	v_pk_add_f32 v[132:133], v[138:139], v[132:133]
	v_pk_add_f32 v[130:131], v[148:149], v[130:131]
	v_pk_add_f32 v[132:133], v[132:133], v[140:141]
	v_pk_add_f32 v[130:131], v[130:131], v[144:145]
	v_mfma_f32_32x32x16_bf16 v[34:49], v[66:69], v[78:81], v[34:49]
	s_waitcnt vmcnt(0) lgkmcnt(0)
	v_mul_f32_e32 v66, v175, v70
	v_add_f32_e32 v130, v131, v130
	v_add_f32_e32 v131, v132, v133
	ds_write_b32 v173, v66 offset:512
	v_mul_f32_e32 v66, v175, v71
	v_add_f32_e32 v130, v130, v131
	s_waitcnt lgkmcnt(0)
	ds_read_b128 v[102:105], v174 offset:34560
	ds_read_b128 v[98:101], v174 offset:34592
	ds_read_b128 v[110:113], v174 offset:34624
	ds_read_b128 v[106:109], v174 offset:34656
	ds_read_b128 v[114:117], v174 offset:34688
	ds_read_b128 v[122:125], v174 offset:34720
	ds_read_b128 v[118:121], v174 offset:34752
	ds_read_b128 v[126:129], v174 offset:34784
	v_mov_b32_dpp v66, v66 quad_perm:[1,0,3,2] row_mask:0xf bank_mask:0xf bound_ctrl:1
	v_mov_b32_e32 v131, v130
	v_fmac_f32_e32 v66, v175, v71
	s_nop 0
	v_permlane32_swap_b32_e32 v130, v131
	v_add_f32_dpp v66, v66, v66 quad_perm:[2,3,0,1] row_mask:0xf bank_mask:0xf bound_ctrl:1
	v_add_f32_e32 v130, v130, v131
	v_fmamk_f32 v65, v130, 0xbc800000, v65
	v_add_f32_dpp v66, v66, v66 row_half_mirror row_mask:0xf bank_mask:0xf bound_ctrl:1
	v_fmamk_f32 v64, v130, 0xbc800000, v64
	v_fmamk_f32 v63, v130, 0xbc800000, v63
	v_fmamk_f32 v62, v130, 0xbc800000, v62
	v_fmamk_f32 v61, v130, 0xbc800000, v61
	v_fmamk_f32 v60, v130, 0xbc800000, v60
	v_fmamk_f32 v59, v130, 0xbc800000, v59
	v_fmamk_f32 v58, v130, 0xbc800000, v58
	v_fmamk_f32 v57, v130, 0xbc800000, v57
	v_fmamk_f32 v56, v130, 0xbc800000, v56
	v_fmamk_f32 v55, v130, 0xbc800000, v55
	v_fmamk_f32 v54, v130, 0xbc800000, v54
	v_fmamk_f32 v53, v130, 0xbc800000, v53
	v_fmamk_f32 v52, v130, 0xbc800000, v52
	v_fmamk_f32 v51, v130, 0xbc800000, v51
	v_fmac_f32_e32 v50, 0xbc800000, v130
	v_add_f32_dpp v66, v66, v66 row_ror:8 row_mask:0xf bank_mask:0xf bound_ctrl:1
	v_fmamk_f32 v17, v130, 0xbc800000, v17
	v_fmamk_f32 v16, v130, 0xbc800000, v16
	v_fmamk_f32 v15, v130, 0xbc800000, v15
	v_fmamk_f32 v14, v130, 0xbc800000, v14
	v_fmamk_f32 v13, v130, 0xbc800000, v13
	v_fmamk_f32 v12, v130, 0xbc800000, v12
	v_fmamk_f32 v11, v130, 0xbc800000, v11
	v_fmamk_f32 v10, v130, 0xbc800000, v10
	v_fmamk_f32 v9, v130, 0xbc800000, v9
	v_fmamk_f32 v8, v130, 0xbc800000, v8
	v_fmamk_f32 v7, v130, 0xbc800000, v7
	v_fmamk_f32 v6, v130, 0xbc800000, v6
	v_fmamk_f32 v5, v130, 0xbc800000, v5
	v_fmamk_f32 v4, v130, 0xbc800000, v4
	v_fmamk_f32 v3, v130, 0xbc800000, v3
	v_fmac_f32_e32 v2, 0xbc800000, v130
	v_pk_mul_f32 v[130:131], v[54:55], v[54:55]
	v_pk_mul_f32 v[132:133], v[62:63], v[62:63]
	v_pk_mul_f32 v[138:139], v[50:51], v[50:51]
	v_pk_mul_f32 v[140:141], v[58:59], v[58:59]
	v_pk_mul_f32 v[142:143], v[56:57], v[56:57]
	v_pk_mul_f32 v[144:145], v[64:65], v[64:65]
	v_pk_mul_f32 v[146:147], v[52:53], v[52:53]
	v_pk_mul_f32 v[148:149], v[60:61], v[60:61]
	v_mov_b32_e32 v67, v66
	v_pk_fma_f32 v[148:149], v[12:13], v[12:13], v[148:149]
	v_pk_fma_f32 v[146:147], v[4:5], v[4:5], v[146:147]
	v_pk_fma_f32 v[144:145], v[16:17], v[16:17], v[144:145]
	v_pk_fma_f32 v[142:143], v[8:9], v[8:9], v[142:143]
	v_pk_fma_f32 v[140:141], v[10:11], v[10:11], v[140:141]
	v_pk_fma_f32 v[138:139], v[2:3], v[2:3], v[138:139]
	v_pk_fma_f32 v[132:133], v[14:15], v[14:15], v[132:133]
	v_pk_fma_f32 v[130:131], v[6:7], v[6:7], v[130:131]
	v_permlane16_swap_b32_e32 v66, v67
	v_pk_add_f32 v[130:131], v[130:131], v[132:133]
	v_pk_add_f32 v[132:133], v[138:139], v[140:141]
	v_pk_add_f32 v[138:139], v[142:143], v[144:145]
	v_pk_add_f32 v[140:141], v[146:147], v[148:149]
	v_mfma_f32_32x32x16_bf16 v[18:33], v[74:77], v[78:81], v[18:33]
	v_add_f32_e32 v136, v66, v67
	ds_read_b128 v[70:73], v134 offset:512
	ds_read_b128 v[66:69], v134 offset:544
	ds_read_b128 v[78:81], v134 offset:576
	ds_read_b128 v[74:77], v134 offset:608
	ds_read_b128 v[82:85], v134 offset:640
	ds_read_b128 v[90:93], v134 offset:672
	ds_read_b128 v[86:89], v134 offset:704
	ds_read_b128 v[94:97], v134 offset:736
	v_pk_add_f32 v[138:139], v[140:141], v[138:139]
	v_pk_add_f32 v[130:131], v[132:133], v[130:131]
	s_waitcnt lgkmcnt(8)
	v_pk_mul_f32 v[140:141], v[126:127], v[62:63]
	v_pk_mov_b32 v[132:133], v[130:131], v[138:139] op_sel:[1,0]
	v_mov_b32_e32 v131, v139
	v_pk_mul_f32 v[138:139], v[122:123], v[54:55]
	v_pk_mul_f32 v[142:143], v[114:115], v[50:51]
	v_pk_mul_f32 v[144:145], v[118:119], v[58:59]
	v_pk_mul_f32 v[146:147], v[124:125], v[56:57]
	v_pk_mul_f32 v[148:149], v[128:129], v[64:65]
	v_pk_mul_f32 v[154:155], v[116:117], v[52:53]
	v_pk_mul_f32 v[156:157], v[120:121], v[60:61]
	v_pk_fma_f32 v[154:155], v[104:105], v[4:5], v[154:155]
	v_pk_fma_f32 v[156:157], v[112:113], v[12:13], v[156:157]
	v_pk_fma_f32 v[148:149], v[108:109], v[16:17], v[148:149]
	v_pk_fma_f32 v[146:147], v[100:101], v[8:9], v[146:147]
	v_pk_fma_f32 v[144:145], v[110:111], v[10:11], v[144:145]
	v_pk_fma_f32 v[142:143], v[102:103], v[2:3], v[142:143]
	v_pk_fma_f32 v[140:141], v[106:107], v[14:15], v[140:141]
	v_pk_fma_f32 v[138:139], v[98:99], v[6:7], v[138:139]
	v_pk_add_f32 v[130:131], v[132:133], v[130:131]
	v_pk_add_f32 v[138:139], v[138:139], v[140:141]
	v_pk_add_f32 v[140:141], v[142:143], v[144:145]
	v_pk_add_f32 v[142:143], v[146:147], v[148:149]
	v_pk_add_f32 v[144:145], v[154:155], v[156:157]
	v_pk_add_f32 v[132:133], v[130:131], v[130:131] op_sel:[0,1] op_sel_hi:[1,0]
	v_pk_add_f32 v[142:143], v[144:145], v[142:143]
	v_pk_add_f32 v[138:139], v[140:141], v[138:139]
	v_add_f32_e32 v133, v142, v143
	v_add_f32_e32 v130, v138, v139
	s_waitcnt lgkmcnt(2)
	v_pk_mul_f32 v[138:139], v[90:91], v[54:55]
	s_waitcnt lgkmcnt(0)
	v_pk_mul_f32 v[140:141], v[94:95], v[62:63]
	v_pk_mul_f32 v[142:143], v[82:83], v[50:51]
	v_pk_mul_f32 v[144:145], v[86:87], v[58:59]
	v_pk_mul_f32 v[146:147], v[92:93], v[56:57]
	v_pk_mul_f32 v[148:149], v[96:97], v[64:65]
	v_pk_mul_f32 v[154:155], v[84:85], v[52:53]
	v_pk_mul_f32 v[156:157], v[88:89], v[60:61]
	v_add_f32_e32 v130, v130, v133
	v_pk_fma_f32 v[156:157], v[80:81], v[12:13], v[156:157]
	v_pk_fma_f32 v[154:155], v[72:73], v[4:5], v[154:155]
	v_pk_fma_f32 v[148:149], v[76:77], v[16:17], v[148:149]
	v_pk_fma_f32 v[146:147], v[68:69], v[8:9], v[146:147]
	v_pk_fma_f32 v[144:145], v[78:79], v[10:11], v[144:145]
	v_pk_fma_f32 v[142:143], v[70:71], v[2:3], v[142:143]
	v_pk_fma_f32 v[140:141], v[74:75], v[14:15], v[140:141]
	v_pk_fma_f32 v[138:139], v[66:67], v[6:7], v[138:139]
	v_mov_b32_e32 v133, v130
	v_pk_add_f32 v[138:139], v[138:139], v[140:141]
	v_pk_add_f32 v[140:141], v[142:143], v[144:145]
	v_pk_add_f32 v[142:143], v[146:147], v[148:149]
	v_pk_add_f32 v[144:145], v[154:155], v[156:157]
	v_permlane32_swap_b32_e32 v130, v133
	v_pk_add_f32 v[142:143], v[144:145], v[142:143]
	v_add_f32_e32 v160, v130, v133
	v_pk_add_f32 v[138:139], v[140:141], v[138:139]
	v_add_f32_e32 v133, v142, v143
	v_pk_add_f32 v[140:141], v[26:27], v[42:43]
	v_pk_add_f32 v[142:143], v[28:29], v[44:45]
	v_pk_add_f32 v[144:145], v[20:21], v[36:37]
	v_pk_add_f32 v[146:147], v[32:33], v[48:49]
	v_pk_add_f32 v[148:149], v[24:25], v[40:41]
	v_pk_add_f32 v[154:155], v[30:31], v[46:47]
	v_pk_add_f32 v[156:157], v[22:23], v[38:39]
	v_pk_add_f32 v[158:159], v[18:19], v[34:35]
	v_pk_add_f32 v[154:155], v[156:157], v[154:155]
	v_pk_add_f32 v[146:147], v[148:149], v[146:147]
	v_pk_add_f32 v[142:143], v[144:145], v[142:143]
	v_pk_add_f32 v[140:141], v[158:159], v[140:141]
	v_pk_add_f32 v[142:143], v[142:143], v[146:147]
	v_pk_add_f32 v[140:141], v[140:141], v[154:155]
	v_add_f32_e32 v130, v138, v139
	v_add_f32_e32 v140, v141, v140
	v_add_f32_e32 v141, v142, v143
	v_add_f32_e32 v133, v130, v133
	v_add_f32_e32 v140, v140, v141
	v_mov_b32_e32 v131, v132
	v_mov_b32_e32 v130, v140
	s_nop 1
	v_permlane32_swap_b32_e32 v140, v130
	v_add_f32_e32 v130, v140, v130
	v_fmamk_f32 v49, v130, 0xbc800000, v49
	v_fmamk_f32 v48, v130, 0xbc800000, v48
	v_fmamk_f32 v47, v130, 0xbc800000, v47
	v_fmamk_f32 v46, v130, 0xbc800000, v46
	v_fmamk_f32 v45, v130, 0xbc800000, v45
	v_fmamk_f32 v44, v130, 0xbc800000, v44
	v_fmamk_f32 v43, v130, 0xbc800000, v43
	v_fmamk_f32 v42, v130, 0xbc800000, v42
	v_fmamk_f32 v41, v130, 0xbc800000, v41
	v_fmamk_f32 v40, v130, 0xbc800000, v40
	v_fmamk_f32 v39, v130, 0xbc800000, v39
	v_fmamk_f32 v38, v130, 0xbc800000, v38
	v_fmamk_f32 v37, v130, 0xbc800000, v37
	v_fmamk_f32 v36, v130, 0xbc800000, v36
	v_fmamk_f32 v35, v130, 0xbc800000, v35
	v_fmac_f32_e32 v34, 0xbc800000, v130
	v_fmamk_f32 v33, v130, 0xbc800000, v33
	v_fmamk_f32 v32, v130, 0xbc800000, v32
	v_fmamk_f32 v31, v130, 0xbc800000, v31
	v_fmamk_f32 v30, v130, 0xbc800000, v30
	v_fmamk_f32 v29, v130, 0xbc800000, v29
	v_fmamk_f32 v28, v130, 0xbc800000, v28
	v_fmamk_f32 v27, v130, 0xbc800000, v27
	v_fmamk_f32 v26, v130, 0xbc800000, v26
	v_fmamk_f32 v25, v130, 0xbc800000, v25
	v_fmamk_f32 v24, v130, 0xbc800000, v24
	v_fmamk_f32 v23, v130, 0xbc800000, v23
	v_fmamk_f32 v22, v130, 0xbc800000, v22
	v_fmamk_f32 v21, v130, 0xbc800000, v21
	v_fmamk_f32 v20, v130, 0xbc800000, v20
	v_fmamk_f32 v19, v130, 0xbc800000, v19
	v_fmac_f32_e32 v18, 0xbc800000, v130
	v_pk_mul_f32 v[140:141], v[38:39], v[38:39]
	v_pk_mul_f32 v[142:143], v[46:47], v[46:47]
	v_pk_mul_f32 v[144:145], v[34:35], v[34:35]
	v_pk_mul_f32 v[146:147], v[42:43], v[42:43]
	v_pk_mul_f32 v[148:149], v[40:41], v[40:41]
	v_pk_mul_f32 v[154:155], v[48:49], v[48:49]
	v_pk_mul_f32 v[156:157], v[36:37], v[36:37]
	v_pk_mul_f32 v[158:159], v[44:45], v[44:45]
	v_pk_fma_f32 v[156:157], v[20:21], v[20:21], v[156:157]
	v_pk_fma_f32 v[158:159], v[28:29], v[28:29], v[158:159]
	v_pk_fma_f32 v[154:155], v[32:33], v[32:33], v[154:155]
	v_pk_fma_f32 v[148:149], v[24:25], v[24:25], v[148:149]
	v_pk_fma_f32 v[146:147], v[26:27], v[26:27], v[146:147]
	v_pk_fma_f32 v[144:145], v[18:19], v[18:19], v[144:145]
	v_pk_fma_f32 v[142:143], v[30:31], v[30:31], v[142:143]
	v_pk_fma_f32 v[140:141], v[22:23], v[22:23], v[140:141]
	v_permlane32_swap_b32_e32 v132, v131
	v_pk_add_f32 v[140:141], v[140:141], v[142:143]
	v_pk_add_f32 v[142:143], v[144:145], v[146:147]
	v_pk_add_f32 v[144:145], v[148:149], v[154:155]
	v_pk_add_f32 v[146:147], v[156:157], v[158:159]
	v_pk_add_f32 v[140:141], v[142:143], v[140:141]
	v_pk_add_f32 v[144:145], v[146:147], v[144:145]
	v_pk_mul_f32 v[122:123], v[122:123], v[38:39]
	v_pk_mov_b32 v[142:143], v[140:141], v[144:145] op_sel:[1,0]
	v_mov_b32_e32 v141, v145
	v_pk_add_f32 v[140:141], v[142:143], v[140:141]
	v_pk_mul_f32 v[126:127], v[126:127], v[46:47]
	v_pk_add_f32 v[140:141], v[140:141], v[140:141] op_sel:[0,1] op_sel_hi:[1,0]
	v_pk_mul_f32 v[114:115], v[114:115], v[34:35]
	v_mov_b32_e32 v130, v140
	s_nop 1
	v_permlane32_swap_b32_e32 v140, v130
	v_mov_b32_e32 v141, v132
	v_pk_add_f32 v[130:131], v[140:141], v[130:131]
	v_pk_mul_f32 v[118:119], v[118:119], v[42:43]
	v_pk_fma_f32 v[130:131], v[130:131], s[0:1], v[152:153] op_sel_hi:[1,0,0]
	v_pk_mul_f32 v[124:125], v[124:125], v[40:41]
	v_pk_mul_f32 v[128:129], v[128:129], v[48:49]
	v_pk_mul_f32 v[116:117], v[116:117], v[36:37]
	v_pk_mul_f32 v[120:121], v[120:121], v[44:45]
	v_pk_fma_f32 v[112:113], v[112:113], v[28:29], v[120:121]
	v_pk_fma_f32 v[104:105], v[104:105], v[20:21], v[116:117]
	v_pk_fma_f32 v[108:109], v[108:109], v[32:33], v[128:129]
	v_pk_fma_f32 v[100:101], v[100:101], v[24:25], v[124:125]
	v_pk_fma_f32 v[110:111], v[110:111], v[26:27], v[118:119]
	v_pk_fma_f32 v[102:103], v[102:103], v[18:19], v[114:115]
	v_pk_fma_f32 v[106:107], v[106:107], v[30:31], v[126:127]
	v_pk_fma_f32 v[98:99], v[98:99], v[22:23], v[122:123]
	v_rsq_f32_e32 v131, v131
	v_pk_add_f32 v[98:99], v[98:99], v[106:107]
	v_pk_add_f32 v[102:103], v[102:103], v[110:111]
	v_pk_add_f32 v[100:101], v[100:101], v[108:109]
	v_pk_add_f32 v[104:105], v[104:105], v[112:113]
	v_rsq_f32_e32 v132, v130
	v_pk_add_f32 v[100:101], v[104:105], v[100:101]
	v_pk_add_f32 v[98:99], v[102:103], v[98:99]
	v_add_f32_e32 v98, v98, v99
	v_add_f32_e32 v99, v100, v101
	v_add_f32_e32 v98, v98, v99
	v_mov_b32_e32 v99, v98
	v_pk_mul_f32 v[90:91], v[90:91], v[38:39]
	v_pk_mul_f32 v[94:95], v[94:95], v[46:47]
	v_pk_mul_f32 v[82:83], v[82:83], v[34:35]
	v_pk_mul_f32 v[86:87], v[86:87], v[42:43]
	v_permlane32_swap_b32_e32 v98, v99
	v_pk_fma_f32 v[78:79], v[78:79], v[26:27], v[86:87]
	v_pk_fma_f32 v[70:71], v[70:71], v[18:19], v[82:83]
	v_pk_fma_f32 v[74:75], v[74:75], v[30:31], v[94:95]
	v_pk_fma_f32 v[66:67], v[66:67], v[22:23], v[90:91]
	v_mov_b32_e32 v130, v131
	v_mov_b32_e32 v131, v132
	v_add_f32_e32 v98, v98, v99
	v_pk_add_f32 v[66:67], v[66:67], v[74:75]
	v_pk_add_f32 v[70:71], v[70:71], v[78:79]
	v_mul_f32_e32 v139, v160, v130
	v_mul_f32_e32 v98, v98, v131
	v_pk_add_f32 v[66:67], v[70:71], v[66:67]
	v_cmp_gt_u32_e32 vcc, 32, v1
	v_add_f32_e32 v66, v66, v67
	v_pk_mul_f32 v[92:93], v[92:93], v[40:41]
	v_cndmask_b32_e32 v67, v98, v139, vcc
	v_add_f32_e32 v67, s12, v67
	v_pk_mul_f32 v[96:97], v[96:97], v[48:49]
	v_pk_mul_f32 v[84:85], v[84:85], v[36:37]
	v_pk_mul_f32 v[88:89], v[88:89], v[44:45]
	v_mul_f32_e32 v67, 0xbfb8aa3b, v67
	v_pk_fma_f32 v[80:81], v[80:81], v[28:29], v[88:89]
	v_pk_fma_f32 v[72:73], v[72:73], v[20:21], v[84:85]
	v_pk_fma_f32 v[76:77], v[76:77], v[32:33], v[96:97]
	v_pk_fma_f32 v[68:69], v[68:69], v[24:25], v[92:93]
	v_exp_f32_e32 v70, v67
	v_pk_add_f32 v[68:69], v[68:69], v[76:77]
	v_pk_add_f32 v[72:73], v[72:73], v[80:81]
	v_cmp_lt_i32_e64 s[0:1], 0, v151
	v_pk_add_f32 v[68:69], v[72:73], v[68:69]
	v_mov_b32_e32 v137, v136
	v_add_f32_e32 v67, v68, v69
	v_add_f32_e32 v67, v66, v67
	v_add_f32_e32 v66, 1.0, v70
	v_rcp_f32_e32 v66, v66
	v_mov_b32_e32 v69, 0xff800000
	v_mov_b32_e32 v138, v133
	v_mov_b32_e32 v68, v67
	v_cndmask_b32_e64 v70, v69, v66, s[0:1]
	v_mbcnt_lo_u32_b32 v66, -1, 0
	v_mbcnt_hi_u32_b32 v66, -1, v66
	v_permlane32_swap_b32_e32 v136, v137
	v_permlane32_swap_b32_e32 v133, v138
	v_permlane32_swap_b32_e32 v67, v68
	v_and_b32_e32 v86, 64, v66
	s_mov_b32 s14, 8
	s_mov_b32 s13, 0
	v_mov_b32_e32 v66, 0
	s_waitcnt lgkmcnt(0)
